# up-projection output: five eighths of H stored with the default cache policy, three eighths nt
# speedup vs baseline: 1.0172x; 1.0172x over previous
; #define PG8_LAS __attribute__((address_space(3)))
; #define PG8_GAS __attribute__((address_space(1)))
; #define PG8_PACK8(y0, y1) (u32x4){cvt_pk_bf16((y0)[0], (y0)[1]), cvt_pk_bf16((y0)[2], (y0)[3]), cvt_pk_bf16((y1)[0], (y1)[1]), cvt_pk_bf16((y1)[2], (y1)[3])}
;     __device__ __forceinline__ void operator()(const f32x4 (&acc)[2][2][4][2], const Unit& u, int ui, int wr, int wc, int fr, int fq) const {
;     ...
;         const unsigned row0 = (unsigned)(u.pm * BM + wr * 64 + fr), colp = (unsigned)((u.pn & 3) * BM + wc * 32 + 8 * fq);
;         const PG8_LAS float* rsp = tab + (u.pm == pmA ? 0 : 256) + wr * 64 + fr;
;         float rsv[2][4];
; #pragma unroll
;         for (int ai = 0; ai < 2; ++ai)
; #pragma unroll
;             for (int m = 0; m < 4; ++m) rsv[ai][m] = rsp[ai * HALF + m * 16];
; #pragma unroll
;         for (int ai = 0; ai < 2; ++ai)
; #pragma unroll
;             for (int m = 0; m < 4; ++m) {
;                 const unsigned row = row0 + ai * HALF + m * 16; const float rs = rsv[ai][m];
; #pragma unroll
;                 for (int bj = 0; bj < 2; ++bj) {
;                     f32x4 y0 = acc[ai][bj][m][0] * rs, y1 = acc[ai][bj][m][1] * rs;
; #pragma unroll
;                     for (int e = 0; e < 4; ++e) { const float a = fmaxf(y0[e], 0.f), b = fmaxf(y1[e], 0.f); y0[e] = a * a; y1[e] = b * b; }
;                     const u32x4 hw = PG8_PACK8(y0, y1);
;     ...
;                     if (probe_mode == 1) { asm volatile("" :: "v"(hw)); } else
;     ...
;                     *(PG8_GAS u32x4*)((PG8_GAS unsigned char*)ws + E_QKVO + (size_t)((unsigned)(u.pm >> 4) * (24u << 20) + (unsigned)(u.pn >> 2) * (8u << 20) + row * 2048u + (colp + bj * HALF) * 2u)) = hw;
.LBB0_64:
	s_lshl_b32 s13, s51, 9
	s_cmp_eq_u32 s20, s29
	s_cselect_b32 s15, 0, 0x400
	v_add_u32_e32 v140, s15, v145
	ds_read2_b32 v[164:165], v140 offset1:16
	ds_read2_b32 v[166:167], v140 offset0:32 offset1:48
	ds_read2_b32 v[142:143], v140 offset0:128 offset1:144
	ds_read2_b32 v[140:141], v140 offset0:160 offset1:176
	s_lshl_b32 s22, s51, 21
	s_lshr_b32 s15, s20, 4
	s_and_b32 s22, s22, 0xff800000
	s_lshl_b32 s20, s20, 19
	s_waitcnt lgkmcnt(0)
	v_pk_mul_f32 v[122:123], v[122:123], v[164:165] op_sel_hi:[1,0]
	s_add_i32 s22, s22, s20
	v_pk_mul_f32 v[126:127], v[126:127], v[164:165] op_sel_hi:[1,0]
	v_pk_mul_f32 v[124:125], v[124:125], v[164:165] op_sel_hi:[1,0]
	v_max_f32_e32 v122, 0, v122
	s_and_b32 s13, s13, 0x600
	v_add_u32_e32 v163, s22, v146
	v_pk_mul_f32 v[128:129], v[128:129], v[164:165] op_sel_hi:[1,0]
	v_mul_f32_e32 v168, v122, v122
	v_max_f32_e32 v122, 0, v127
	v_max_f32_e32 v123, 0, v123
	v_max_f32_e32 v124, 0, v124
	s_mul_i32 s15, s15, 0x1800000
	v_or_b32_e32 v163, s13, v163
	v_max_f32_e32 v126, 0, v126
	v_mul_f32_e32 v122, v122, v122
	v_mul_f32_e32 v127, v123, v123
	v_max_f32_e32 v123, 0, v128
	v_mul_f32_e32 v128, v124, v124
	v_max_f32_e32 v124, 0, v129
	v_max_f32_e32 v125, 0, v125
	v_pk_mul_f32 v[114:115], v[114:115], v[164:165] op_sel_hi:[1,0]
	v_add_u32_e32 v163, s15, v163
	v_mul_f32_e32 v126, v126, v126
	v_mul_f32_e32 v123, v123, v123
	v_mul_f32_e32 v124, v124, v124
	v_mul_f32_e32 v125, v125, v125
	v_cvt_pk_bf16_f32 v122, v126, v122
	v_pk_mul_f32 v[120:121], v[120:121], v[164:165] op_sel_hi:[1,0]
	v_pk_mul_f32 v[118:119], v[118:119], v[164:165] op_sel_hi:[1,0]
	v_pk_mul_f32 v[116:117], v[116:117], v[164:165] op_sel_hi:[1,0]
	v_max_f32_e32 v114, 0, v114
	v_max_f32_e32 v115, 0, v115
	v_cvt_pk_bf16_f32 v123, v123, v124
	v_cvt_pk_bf16_f32 v124, v168, v127
	v_cvt_pk_bf16_f32 v125, v128, v125
	global_store_dwordx4 v163, v[122:125], s[10:11] nt
	v_max_f32_e32 v118, 0, v118
	v_max_f32_e32 v116, 0, v116
	v_mul_f32_e32 v122, v114, v114
	v_max_f32_e32 v114, 0, v119
	v_mul_f32_e32 v119, v115, v115
	v_max_f32_e32 v115, 0, v120
	v_mul_f32_e32 v118, v118, v118
	v_mul_f32_e32 v114, v114, v114
	v_mul_f32_e32 v115, v115, v115
	v_mul_f32_e32 v120, v116, v116
	v_max_f32_e32 v116, 0, v121
	v_max_f32_e32 v117, 0, v117
	v_mul_f32_e32 v116, v116, v116
	v_mul_f32_e32 v117, v117, v117
	v_cvt_pk_bf16_f32 v114, v118, v114
	v_cvt_pk_bf16_f32 v115, v115, v116
	v_or_b32_e32 v118, 0x100, v163
	v_cvt_pk_bf16_f32 v116, v122, v119
	v_cvt_pk_bf16_f32 v117, v120, v117
	global_store_dwordx4 v118, v[114:117], s[10:11] nt
	v_pk_mul_f32 v[90:91], v[90:91], v[166:167] op_sel_hi:[1,0]
	v_pk_mul_f32 v[94:95], v[94:95], v[166:167] op_sel_hi:[1,0]
	v_or_b32_e32 v115, 0x8000, v163
	v_mov_b32_e32 v114, v165
	v_pk_mul_f32 v[106:107], v[106:107], v[114:115] op_sel_hi:[1,0]
	v_pk_mul_f32 v[110:111], v[110:111], v[114:115] op_sel_hi:[1,0]
	v_pk_mul_f32 v[108:109], v[108:109], v[114:115] op_sel_hi:[1,0]
	v_max_f32_e32 v106, 0, v106
	v_pk_mul_f32 v[112:113], v[112:113], v[114:115] op_sel_hi:[1,0]
	v_mul_f32_e32 v116, v106, v106
	v_max_f32_e32 v106, 0, v111
	v_max_f32_e32 v107, 0, v107
	v_max_f32_e32 v108, 0, v108
	v_max_f32_e32 v110, 0, v110
	v_mul_f32_e32 v106, v106, v106
	v_mul_f32_e32 v111, v107, v107
	v_max_f32_e32 v107, 0, v112
	v_mul_f32_e32 v112, v108, v108
	v_max_f32_e32 v108, 0, v113
	v_max_f32_e32 v109, 0, v109
	v_pk_mul_f32 v[98:99], v[98:99], v[114:115] op_sel_hi:[1,0]
	v_mul_f32_e32 v110, v110, v110
	v_mul_f32_e32 v107, v107, v107
	v_mul_f32_e32 v108, v108, v108
	v_mul_f32_e32 v109, v109, v109
	v_cvt_pk_bf16_f32 v106, v110, v106
	v_pk_mul_f32 v[104:105], v[104:105], v[114:115] op_sel_hi:[1,0]
	v_pk_mul_f32 v[102:103], v[102:103], v[114:115] op_sel_hi:[1,0]
	v_pk_mul_f32 v[100:101], v[100:101], v[114:115] op_sel_hi:[1,0]
	v_max_f32_e32 v98, 0, v98
	v_max_f32_e32 v99, 0, v99
	v_cvt_pk_bf16_f32 v107, v107, v108
	v_cvt_pk_bf16_f32 v108, v116, v111
	v_cvt_pk_bf16_f32 v109, v112, v109
	global_store_dwordx4 v115, v[106:109], s[10:11] nt
	v_max_f32_e32 v102, 0, v102
	v_max_f32_e32 v100, 0, v100
	v_mul_f32_e32 v106, v98, v98
	v_max_f32_e32 v98, 0, v103
	v_mul_f32_e32 v103, v99, v99
	v_max_f32_e32 v99, 0, v104
	v_mul_f32_e32 v102, v102, v102
	v_mul_f32_e32 v98, v98, v98
	v_mul_f32_e32 v99, v99, v99
	v_mul_f32_e32 v104, v100, v100
	v_max_f32_e32 v100, 0, v105
	v_max_f32_e32 v101, 0, v101
	v_mul_f32_e32 v100, v100, v100
	v_mul_f32_e32 v101, v101, v101
	v_cvt_pk_bf16_f32 v98, v102, v98
	v_cvt_pk_bf16_f32 v99, v99, v100
	v_or_b32_e32 v102, 0x8100, v163
	v_pk_mul_f32 v[92:93], v[92:93], v[166:167] op_sel_hi:[1,0]
	v_max_f32_e32 v90, 0, v90
	v_cvt_pk_bf16_f32 v100, v106, v103
	v_cvt_pk_bf16_f32 v101, v104, v101
	global_store_dwordx4 v102, v[98:101], s[10:11] nt
	v_pk_mul_f32 v[96:97], v[96:97], v[166:167] op_sel_hi:[1,0]
	v_max_f32_e32 v91, 0, v91
	v_mul_f32_e32 v99, v90, v90
	v_max_f32_e32 v90, 0, v95
	v_max_f32_e32 v92, 0, v92
	v_max_f32_e32 v94, 0, v94
	v_mul_f32_e32 v90, v90, v90
	v_mul_f32_e32 v95, v91, v91
	v_max_f32_e32 v91, 0, v96
	v_mul_f32_e32 v96, v92, v92
	v_max_f32_e32 v92, 0, v97
	v_max_f32_e32 v93, 0, v93
	v_pk_mul_f32 v[82:83], v[82:83], v[166:167] op_sel_hi:[1,0]
	v_or_b32_e32 v98, 0x10000, v163
	v_mul_f32_e32 v94, v94, v94
	v_mul_f32_e32 v91, v91, v91
	v_mul_f32_e32 v92, v92, v92
	v_mul_f32_e32 v93, v93, v93
	v_cvt_pk_bf16_f32 v90, v94, v90
	v_pk_mul_f32 v[88:89], v[88:89], v[166:167] op_sel_hi:[1,0]
	v_pk_mul_f32 v[86:87], v[86:87], v[166:167] op_sel_hi:[1,0]
	v_pk_mul_f32 v[84:85], v[84:85], v[166:167] op_sel_hi:[1,0]
	v_max_f32_e32 v82, 0, v82
	v_max_f32_e32 v83, 0, v83
	v_cvt_pk_bf16_f32 v91, v91, v92
	v_cvt_pk_bf16_f32 v92, v99, v95
	v_cvt_pk_bf16_f32 v93, v96, v93
; #define PG8_GAS __attribute__((address_space(1)))
; #define PG8_PACK8(y0, y1) (u32x4){cvt_pk_bf16((y0)[0], (y0)[1]), cvt_pk_bf16((y0)[2], (y0)[3]), cvt_pk_bf16((y1)[0], (y1)[1]), cvt_pk_bf16((y1)[2], (y1)[3])}
;     __device__ __forceinline__ void operator()(const f32x4 (&acc)[2][2][4][2], const Unit& u, int ui, int wr, int wc, int fr, int fq) const {
;     ...
;         for (int ai = 0; ai < 2; ++ai)
; #pragma unroll
;             for (int m = 0; m < 4; ++m) {
;                 const unsigned row = row0 + ai * HALF + m * 16; const float rs = rsv[ai][m];
; #pragma unroll
;                 for (int bj = 0; bj < 2; ++bj) {
;                     f32x4 y0 = acc[ai][bj][m][0] * rs, y1 = acc[ai][bj][m][1] * rs;
; #pragma unroll
;                     for (int e = 0; e < 4; ++e) { const float a = fmaxf(y0[e], 0.f), b = fmaxf(y1[e], 0.f); y0[e] = a * a; y1[e] = b * b; }
;                     const u32x4 hw = PG8_PACK8(y0, y1);
;     ...
;                     if (probe_mode == 1) { asm volatile("" :: "v"(hw)); } else
;     ...
;                     *(PG8_GAS u32x4*)((PG8_GAS unsigned char*)ws + E_QKVO + (size_t)((unsigned)(u.pm >> 4) * (24u << 20) + (unsigned)(u.pn >> 2) * (8u << 20) + row * 2048u + (colp + bj * HALF) * 2u)) = hw;
	global_store_dwordx4 v98, v[90:93], s[10:11] nt
	v_max_f32_e32 v86, 0, v86
	v_max_f32_e32 v84, 0, v84
	v_mul_f32_e32 v90, v82, v82
	v_max_f32_e32 v82, 0, v87
	v_mul_f32_e32 v87, v83, v83
	v_max_f32_e32 v83, 0, v88
	v_mul_f32_e32 v86, v86, v86
	v_mul_f32_e32 v82, v82, v82
	v_mul_f32_e32 v83, v83, v83
	v_mul_f32_e32 v88, v84, v84
	v_max_f32_e32 v84, 0, v89
	v_max_f32_e32 v85, 0, v85
	v_mul_f32_e32 v84, v84, v84
	v_mul_f32_e32 v85, v85, v85
	v_cvt_pk_bf16_f32 v82, v86, v82
	v_cvt_pk_bf16_f32 v83, v83, v84
	v_or_b32_e32 v86, 0x10100, v163
	v_cvt_pk_bf16_f32 v84, v90, v87
	v_cvt_pk_bf16_f32 v85, v88, v85
	global_store_dwordx4 v86, v[82:85], s[10:11] nt
	v_pk_mul_f32 v[58:59], v[58:59], v[142:143] op_sel_hi:[1,0]
	v_pk_mul_f32 v[62:63], v[62:63], v[142:143] op_sel_hi:[1,0]
	v_or_b32_e32 v83, 0x18000, v163
	v_mov_b32_e32 v82, v167
	v_pk_mul_f32 v[74:75], v[74:75], v[82:83] op_sel_hi:[1,0]
	v_pk_mul_f32 v[78:79], v[78:79], v[82:83] op_sel_hi:[1,0]
	v_pk_mul_f32 v[76:77], v[76:77], v[82:83] op_sel_hi:[1,0]
	v_max_f32_e32 v74, 0, v74
	v_pk_mul_f32 v[80:81], v[80:81], v[82:83] op_sel_hi:[1,0]
	v_mul_f32_e32 v84, v74, v74
	v_max_f32_e32 v74, 0, v79
	v_max_f32_e32 v75, 0, v75
	v_max_f32_e32 v76, 0, v76
	v_max_f32_e32 v78, 0, v78
	v_mul_f32_e32 v74, v74, v74
	v_mul_f32_e32 v79, v75, v75
	v_max_f32_e32 v75, 0, v80
	v_mul_f32_e32 v80, v76, v76
	v_max_f32_e32 v76, 0, v81
	v_max_f32_e32 v77, 0, v77
	v_pk_mul_f32 v[66:67], v[66:67], v[82:83] op_sel_hi:[1,0]
	v_mul_f32_e32 v78, v78, v78
	v_mul_f32_e32 v75, v75, v75
	v_mul_f32_e32 v76, v76, v76
	v_mul_f32_e32 v77, v77, v77
	v_cvt_pk_bf16_f32 v74, v78, v74
	v_pk_mul_f32 v[72:73], v[72:73], v[82:83] op_sel_hi:[1,0]
	v_pk_mul_f32 v[70:71], v[70:71], v[82:83] op_sel_hi:[1,0]
	v_pk_mul_f32 v[68:69], v[68:69], v[82:83] op_sel_hi:[1,0]
	v_max_f32_e32 v66, 0, v66
	v_max_f32_e32 v67, 0, v67
	v_cvt_pk_bf16_f32 v75, v75, v76
	v_cvt_pk_bf16_f32 v76, v84, v79
	v_cvt_pk_bf16_f32 v77, v80, v77
	global_store_dwordx4 v83, v[74:77], s[10:11]
	v_max_f32_e32 v70, 0, v70
	v_max_f32_e32 v68, 0, v68
	v_mul_f32_e32 v74, v66, v66
	v_max_f32_e32 v66, 0, v71
	v_mul_f32_e32 v71, v67, v67
	v_max_f32_e32 v67, 0, v72
	v_mul_f32_e32 v70, v70, v70
	v_mul_f32_e32 v66, v66, v66
	v_mul_f32_e32 v67, v67, v67
	v_mul_f32_e32 v72, v68, v68
	v_max_f32_e32 v68, 0, v73
	v_max_f32_e32 v69, 0, v69
	v_mul_f32_e32 v68, v68, v68
	v_mul_f32_e32 v69, v69, v69
	v_cvt_pk_bf16_f32 v66, v70, v66
	v_cvt_pk_bf16_f32 v67, v67, v68
	v_or_b32_e32 v70, 0x18100, v163
	v_pk_mul_f32 v[60:61], v[60:61], v[142:143] op_sel_hi:[1,0]
	v_max_f32_e32 v58, 0, v58
	v_cvt_pk_bf16_f32 v68, v74, v71
	v_cvt_pk_bf16_f32 v69, v72, v69
	global_store_dwordx4 v70, v[66:69], s[10:11]
	v_pk_mul_f32 v[64:65], v[64:65], v[142:143] op_sel_hi:[1,0]
	v_max_f32_e32 v59, 0, v59
	v_mul_f32_e32 v67, v58, v58
	v_max_f32_e32 v58, 0, v63
	v_max_f32_e32 v60, 0, v60
	v_max_f32_e32 v62, 0, v62
	v_mul_f32_e32 v58, v58, v58
	v_mul_f32_e32 v63, v59, v59
	v_max_f32_e32 v59, 0, v64
	v_mul_f32_e32 v64, v60, v60
	v_max_f32_e32 v60, 0, v65
	v_max_f32_e32 v61, 0, v61
	v_pk_mul_f32 v[50:51], v[50:51], v[142:143] op_sel_hi:[1,0]
	v_add_u32_e32 v66, 0x40000, v163
	v_mul_f32_e32 v62, v62, v62
	v_mul_f32_e32 v59, v59, v59
	v_mul_f32_e32 v60, v60, v60
	v_mul_f32_e32 v61, v61, v61
	v_cvt_pk_bf16_f32 v58, v62, v58
	v_pk_mul_f32 v[56:57], v[56:57], v[142:143] op_sel_hi:[1,0]
	v_pk_mul_f32 v[54:55], v[54:55], v[142:143] op_sel_hi:[1,0]
	v_pk_mul_f32 v[52:53], v[52:53], v[142:143] op_sel_hi:[1,0]
	v_max_f32_e32 v50, 0, v50
	v_max_f32_e32 v51, 0, v51
	v_cvt_pk_bf16_f32 v59, v59, v60
	v_cvt_pk_bf16_f32 v60, v67, v63
	v_cvt_pk_bf16_f32 v61, v64, v61
	global_store_dwordx4 v66, v[58:61], s[10:11]
	v_max_f32_e32 v54, 0, v54
	v_max_f32_e32 v52, 0, v52
	v_mul_f32_e32 v58, v50, v50
	v_max_f32_e32 v50, 0, v55
	v_mul_f32_e32 v55, v51, v51
	v_max_f32_e32 v51, 0, v56
	v_mul_f32_e32 v54, v54, v54
	v_mul_f32_e32 v50, v50, v50
	v_mul_f32_e32 v51, v51, v51
	v_mul_f32_e32 v56, v52, v52
	v_max_f32_e32 v52, 0, v57
	v_max_f32_e32 v53, 0, v53
	v_mul_f32_e32 v52, v52, v52
	v_mul_f32_e32 v53, v53, v53
	v_cvt_pk_bf16_f32 v50, v54, v50
	v_cvt_pk_bf16_f32 v51, v51, v52
	v_add_u32_e32 v54, 0x40100, v163
	v_cvt_pk_bf16_f32 v52, v58, v55
	v_cvt_pk_bf16_f32 v53, v56, v53
	global_store_dwordx4 v54, v[50:53], s[10:11]
	v_pk_mul_f32 v[26:27], v[26:27], v[140:141] op_sel_hi:[1,0]
	v_pk_mul_f32 v[30:31], v[30:31], v[140:141] op_sel_hi:[1,0]
	v_add_u32_e32 v51, 0x48000, v163
	v_mov_b32_e32 v50, v143
	v_pk_mul_f32 v[42:43], v[42:43], v[50:51] op_sel_hi:[1,0]
	v_pk_mul_f32 v[46:47], v[46:47], v[50:51] op_sel_hi:[1,0]
	v_pk_mul_f32 v[44:45], v[44:45], v[50:51] op_sel_hi:[1,0]
	v_max_f32_e32 v42, 0, v42
	v_pk_mul_f32 v[48:49], v[48:49], v[50:51] op_sel_hi:[1,0]
	v_mul_f32_e32 v52, v42, v42
	v_max_f32_e32 v42, 0, v47
	v_max_f32_e32 v43, 0, v43
	v_max_f32_e32 v44, 0, v44
	v_max_f32_e32 v46, 0, v46
	v_mul_f32_e32 v42, v42, v42
	v_mul_f32_e32 v47, v43, v43
; #define PG8_GAS __attribute__((address_space(1)))
; #define PG8_PACK8(y0, y1) (u32x4){cvt_pk_bf16((y0)[0], (y0)[1]), cvt_pk_bf16((y0)[2], (y0)[3]), cvt_pk_bf16((y1)[0], (y1)[1]), cvt_pk_bf16((y1)[2], (y1)[3])}
; #define PG8_BAR __builtin_amdgcn_s_barrier()
;     __device__ __forceinline__ void operator()(const f32x4 (&acc)[2][2][4][2], const Unit& u, int ui, int wr, int wc, int fr, int fq) const {
;     ...
;         for (int ai = 0; ai < 2; ++ai)
; #pragma unroll
;             for (int m = 0; m < 4; ++m) {
;                 const unsigned row = row0 + ai * HALF + m * 16; const float rs = rsv[ai][m];
; #pragma unroll
;                 for (int bj = 0; bj < 2; ++bj) {
;                     f32x4 y0 = acc[ai][bj][m][0] * rs, y1 = acc[ai][bj][m][1] * rs;
; #pragma unroll
;                     for (int e = 0; e < 4; ++e) { const float a = fmaxf(y0[e], 0.f), b = fmaxf(y1[e], 0.f); y0[e] = a * a; y1[e] = b * b; }
;                     const u32x4 hw = PG8_PACK8(y0, y1);
;     ...
;                     if (probe_mode == 1) { asm volatile("" :: "v"(hw)); } else
;     ...
;                     *(PG8_GAS u32x4*)((PG8_GAS unsigned char*)ws + E_QKVO + (size_t)((unsigned)(u.pm >> 4) * (24u << 20) + (unsigned)(u.pn >> 2) * (8u << 20) + row * 2048u + (colp + bj * HALF) * 2u)) = hw;
; template <class Epi, class Sched, bool ALIGN_EPI = false, bool SP2 = false>
; __device__ __forceinline__ void gemm_phase(PG8_LAS unsigned char* lds, const Gemm g, const Sched& S, const Epi& E, const int tid) {
;     ...
;         if (!has_next) break;
; #pragma unroll
;         for (int a = 0; a < 2; ++a)
; #pragma unroll
;             for (int b = 0; b < 2; ++b)
; #pragma unroll
;                 for (int m = 0; m < 4; ++m)
; #pragma unroll
;                     for (int n = 0; n < 2; ++n) acc[a][b][m][n] = (f32x4){0.f, 0.f, 0.f, 0.f};
;         cur = nxt; cA = nA; cB = nB; ++ui;
;         if constexpr (ALIGN_EPI) { if (wr == 1) PG8_BAR; }
	v_max_f32_e32 v43, 0, v48
	v_mul_f32_e32 v48, v44, v44
	v_max_f32_e32 v44, 0, v49
	v_max_f32_e32 v45, 0, v45
	v_pk_mul_f32 v[34:35], v[34:35], v[50:51] op_sel_hi:[1,0]
	v_mul_f32_e32 v46, v46, v46
	v_mul_f32_e32 v43, v43, v43
	v_mul_f32_e32 v44, v44, v44
	v_mul_f32_e32 v45, v45, v45
	v_cvt_pk_bf16_f32 v42, v46, v42
	v_pk_mul_f32 v[40:41], v[40:41], v[50:51] op_sel_hi:[1,0]
	v_pk_mul_f32 v[38:39], v[38:39], v[50:51] op_sel_hi:[1,0]
	v_pk_mul_f32 v[36:37], v[36:37], v[50:51] op_sel_hi:[1,0]
	v_max_f32_e32 v34, 0, v34
	v_max_f32_e32 v35, 0, v35
	v_cvt_pk_bf16_f32 v43, v43, v44
	v_cvt_pk_bf16_f32 v44, v52, v47
	v_cvt_pk_bf16_f32 v45, v48, v45
	global_store_dwordx4 v51, v[42:45], s[10:11]
	v_max_f32_e32 v38, 0, v38
	v_max_f32_e32 v36, 0, v36
	v_mul_f32_e32 v42, v34, v34
	v_max_f32_e32 v34, 0, v39
	v_mul_f32_e32 v39, v35, v35
	v_max_f32_e32 v35, 0, v40
	v_mul_f32_e32 v38, v38, v38
	v_mul_f32_e32 v34, v34, v34
	v_mul_f32_e32 v35, v35, v35
	v_mul_f32_e32 v40, v36, v36
	v_max_f32_e32 v36, 0, v41
	v_max_f32_e32 v37, 0, v37
	v_mul_f32_e32 v36, v36, v36
	v_mul_f32_e32 v37, v37, v37
	v_cvt_pk_bf16_f32 v34, v38, v34
	v_cvt_pk_bf16_f32 v35, v35, v36
	v_add_u32_e32 v38, 0x48100, v163
	v_pk_mul_f32 v[28:29], v[28:29], v[140:141] op_sel_hi:[1,0]
	v_max_f32_e32 v26, 0, v26
	v_cvt_pk_bf16_f32 v36, v42, v39
	v_cvt_pk_bf16_f32 v37, v40, v37
	global_store_dwordx4 v38, v[34:37], s[10:11]
	v_pk_mul_f32 v[32:33], v[32:33], v[140:141] op_sel_hi:[1,0]
	v_max_f32_e32 v27, 0, v27
	v_mul_f32_e32 v35, v26, v26
	v_max_f32_e32 v26, 0, v31
	v_max_f32_e32 v28, 0, v28
	v_max_f32_e32 v30, 0, v30
	v_mul_f32_e32 v26, v26, v26
	v_mul_f32_e32 v31, v27, v27
	v_max_f32_e32 v27, 0, v32
	v_mul_f32_e32 v32, v28, v28
	v_max_f32_e32 v28, 0, v33
	v_max_f32_e32 v29, 0, v29
	v_pk_mul_f32 v[18:19], v[18:19], v[140:141] op_sel_hi:[1,0]
	v_add_u32_e32 v34, 0x50000, v163
	v_mul_f32_e32 v30, v30, v30
	v_mul_f32_e32 v27, v27, v27
	v_mul_f32_e32 v28, v28, v28
	v_mul_f32_e32 v29, v29, v29
	v_cvt_pk_bf16_f32 v26, v30, v26
	v_pk_mul_f32 v[24:25], v[24:25], v[140:141] op_sel_hi:[1,0]
	v_pk_mul_f32 v[22:23], v[22:23], v[140:141] op_sel_hi:[1,0]
	v_pk_mul_f32 v[20:21], v[20:21], v[140:141] op_sel_hi:[1,0]
	v_max_f32_e32 v18, 0, v18
	v_max_f32_e32 v19, 0, v19
	v_cvt_pk_bf16_f32 v27, v27, v28
	v_cvt_pk_bf16_f32 v28, v35, v31
	v_cvt_pk_bf16_f32 v29, v32, v29
	global_store_dwordx4 v34, v[26:29], s[10:11]
	v_max_f32_e32 v22, 0, v22
	v_max_f32_e32 v20, 0, v20
	v_mul_f32_e32 v26, v18, v18
	v_max_f32_e32 v18, 0, v23
	v_mul_f32_e32 v23, v19, v19
	v_max_f32_e32 v19, 0, v24
	v_mul_f32_e32 v22, v22, v22
	v_mul_f32_e32 v18, v18, v18
	v_mul_f32_e32 v19, v19, v19
	v_mul_f32_e32 v24, v20, v20
	v_max_f32_e32 v20, 0, v25
	v_max_f32_e32 v21, 0, v21
	v_mul_f32_e32 v20, v20, v20
	v_mul_f32_e32 v21, v21, v21
	v_cvt_pk_bf16_f32 v18, v22, v18
	v_cvt_pk_bf16_f32 v19, v19, v20
	v_add_u32_e32 v22, 0x50100, v163
	v_cvt_pk_bf16_f32 v20, v26, v23
	v_cvt_pk_bf16_f32 v21, v24, v21
	global_store_dwordx4 v22, v[18:21], s[10:11]
	s_andn2_b64 vcc, exec, s[0:1]
	s_mov_b64 s[0:1], -1
	v_add_u32_e32 v19, 0x58000, v163
	v_mov_b32_e32 v18, v141
	v_pk_mul_f32 v[10:11], v[10:11], v[18:19] op_sel_hi:[1,0]
	v_pk_mul_f32 v[14:15], v[14:15], v[18:19] op_sel_hi:[1,0]
	v_pk_mul_f32 v[12:13], v[12:13], v[18:19] op_sel_hi:[1,0]
	v_max_f32_e32 v10, 0, v10
	v_pk_mul_f32 v[16:17], v[16:17], v[18:19] op_sel_hi:[1,0]
	v_mul_f32_e32 v20, v10, v10
	v_max_f32_e32 v10, 0, v15
	v_max_f32_e32 v11, 0, v11
	v_max_f32_e32 v12, 0, v12
	v_max_f32_e32 v14, 0, v14
	v_mul_f32_e32 v10, v10, v10
	v_mul_f32_e32 v15, v11, v11
	v_max_f32_e32 v11, 0, v16
	v_mul_f32_e32 v16, v12, v12
	v_max_f32_e32 v12, 0, v17
	v_max_f32_e32 v13, 0, v13
	v_pk_mul_f32 v[2:3], v[2:3], v[18:19] op_sel_hi:[1,0]
	v_mul_f32_e32 v14, v14, v14
	v_mul_f32_e32 v11, v11, v11
	v_mul_f32_e32 v12, v12, v12
	v_mul_f32_e32 v13, v13, v13
	v_cvt_pk_bf16_f32 v10, v14, v10
	v_pk_mul_f32 v[6:7], v[6:7], v[18:19] op_sel_hi:[1,0]
	v_pk_mul_f32 v[4:5], v[4:5], v[18:19] op_sel_hi:[1,0]
	v_max_f32_e32 v2, 0, v2
	v_cvt_pk_bf16_f32 v11, v11, v12
	v_cvt_pk_bf16_f32 v12, v20, v15
	v_cvt_pk_bf16_f32 v13, v16, v13
	global_store_dwordx4 v19, v[10:13], s[10:11]
	v_pk_mul_f32 v[8:9], v[8:9], v[18:19] op_sel_hi:[1,0]
	v_max_f32_e32 v6, 0, v6
	v_mul_f32_e32 v10, v2, v2
	v_max_f32_e32 v2, 0, v7
	v_max_f32_e32 v3, 0, v3
	v_max_f32_e32 v4, 0, v4
	v_mul_f32_e32 v6, v6, v6
	v_mul_f32_e32 v2, v2, v2
	v_mul_f32_e32 v7, v3, v3
	v_max_f32_e32 v3, 0, v8
	v_mul_f32_e32 v8, v4, v4
	v_max_f32_e32 v4, 0, v9
	v_max_f32_e32 v5, 0, v5
	v_mul_f32_e32 v3, v3, v3
	v_mul_f32_e32 v4, v4, v4
	v_mul_f32_e32 v5, v5, v5
	v_cvt_pk_bf16_f32 v2, v6, v2
	v_add_u32_e32 v6, 0x58100, v163
	v_cvt_pk_bf16_f32 v3, v3, v4
	v_cvt_pk_bf16_f32 v4, v10, v7
	v_cvt_pk_bf16_f32 v5, v8, v5
	global_store_dwordx4 v6, v[2:5], s[10:11]
	s_mov_b32 s100, 2
	s_cbranch_vccnz .LBB0_53
	s_andn2_b64 vcc, exec, s[6:7]
	s_cbranch_vccnz .LBB0_52
	s_barrier
	s_branch .LBB0_52
